# baseline (speedup 1.0000x reference)
.Lattn_unit:
	s_load_dwordx4 s[4:7], s[0:1], 0x0
	s_lshr_b32 s0, s2, 2
	s_and_b32 s3, s2, 7
	s_and_b32 s0, s0, 8
	s_or_b32 s30, s0, s3
	s_lshr_b32 s18, s2, 6
	s_mov_b32 s19, 0
	s_lshl_b32 s0, s2, 5
	v_readfirstlane_b32 s16, v0
	s_and_b32 s12, s0, 0x300
	s_xor_b32 s12, s12, s91
	s_lshl_b64 s[8:9], s[18:19], 15
	s_lshl_b32 s0, s30, 11
	s_lshr_b32 s33, s16, 6
	s_bfe_u32 s47, s16, 0x10008
	s_or_b32 s8, s8, s0
	s_or_b32 s0, s8, s12
	s_lshl_b32 s31, s33, 5
	s_add_u32 s0, s0, s31
	s_addc_u32 s1, s9, 0
	s_lshl_b64 s[0:1], s[0:1], 7
	s_waitcnt lgkmcnt(0)
	s_add_u32 s0, s4, s0
	s_addc_u32 s1, s5, s1
	s_lshl_b64 s[10:11], s[8:9], 7
	v_bfe_u32 v190, v0, 3, 3
	s_add_u32 s10, s4, s10
	v_lshl_or_b32 v182, s33, 3, v190
	s_addc_u32 s11, s5, s11
	v_lshrrev_b32_e32 v89, 1, v182
	s_add_u32 s14, s10, 0x1000000
	v_xor_b32_e32 v4, v89, v0
	s_addc_u32 s15, s11, 0
	v_mov_b32_e32 v183, 0
	v_lshlrev_b32_e32 v4, 4, v4
	s_add_u32 s10, s10, 0x2000000
	v_lshlrev_b64 v[86:87], 7, v[182:183]
	v_and_b32_e32 v1, 7, v0
	v_and_b32_e32 v182, 0x70, v4
	v_lshrrev_b32_e32 v4, 2, v0
	s_addc_u32 s11, s11, 0
	v_lshl_add_u64 v[2:3], s[14:15], 0, v[86:87]
	v_bitop3_b32 v4, v4, v1, 4 bitop3:0x6c
	v_lshl_add_u64 v[186:187], v[2:3], 0, v[182:183]
	v_lshl_add_u64 v[2:3], s[10:11], 0, v[86:87]
	v_lshlrev_b32_e32 v182, 4, v4
	s_lshl_b32 s36, s33, 10
	s_mov_b32 s13, m0
	s_mov_b32 m0, s36
	s_nop 0
	global_load_lds_dwordx4 v[186:187], off
	s_mov_b32 m0, s13
	s_mov_b64 s[20:21], 0x2000
	v_and_b32_e32 v191, 31, v0
	v_lshl_add_u64 v[194:195], v[2:3], 0, v[182:183]
	s_add_i32 s35, s36, 0x6000
	s_mov_b32 s13, m0
	s_mov_b32 m0, s35
	s_nop 0
	global_load_lds_dwordx4 v[194:195], off
	s_mov_b32 m0, s13
	v_lshl_add_u64 v[2:3], v[186:187], 0, s[20:21]
	v_bfe_u32 v88, v0, 5, 1
	s_add_i32 s37, s36, 0x2000
	s_mov_b32 s13, m0
	s_mov_b32 m0, s37
	s_nop 0
	global_load_lds_dwordx4 v[2:3], off
	s_mov_b32 m0, s13
	v_lshlrev_b32_e32 v2, 6, v191
	v_lshl_or_b32 v192, v88, 3, v2
	v_lshlrev_b32_e32 v14, 1, v192
	global_load_dwordx4 v[154:157], v14, s[0:1]
	global_load_dwordx4 v[146:149], v14, s[0:1] offset:32
	global_load_dwordx4 v[138:141], v14, s[0:1] offset:64
	global_load_dwordx4 v[134:137], v14, s[0:1] offset:96
	v_lshrrev_b32_e32 v18, 1, v0
	s_mov_b64 s[22:23], 0x4000
	v_mov_b32_e32 v2, v183
	v_mov_b32_e32 v3, v183
	v_mov_b32_e32 v4, v183
	v_mov_b32_e32 v5, v183
	v_mov_b32_e32 v6, v183
	v_mov_b32_e32 v7, v183
	v_mov_b32_e32 v8, v183
	v_mov_b32_e32 v9, v183
	v_mov_b32_e32 v10, v183
	v_mov_b32_e32 v11, v183
	v_mov_b32_e32 v12, v183
	v_mov_b32_e32 v13, v183
	v_mov_b32_e32 v14, v183
	v_mov_b32_e32 v15, v183
	v_mov_b32_e32 v16, v183
	v_mov_b32_e32 v17, v183
	v_lshlrev_b32_e32 v38, 7, v191
	v_bitop3_b32 v18, v88, v18, 7 bitop3:0x78
	v_lshl_or_b32 v211, v18, 4, v38
	v_lshl_add_u64 v[18:19], v[186:187], 0, s[22:23]
	s_add_i32 s0, s36, 0x4000
	s_mov_b32 s1, m0
	s_mov_b32 m0, s0
	s_nop 0
	global_load_lds_dwordx4 v[18:19], off
	s_mov_b32 m0, s1
	s_waitcnt vmcnt(3) lgkmcnt(0)
	s_barrier
	ds_read_b128 v[34:37], v211
	v_bfe_u32 v39, v0, 1, 3
	v_bitop3_b32 v40, v88, v39, 2 bitop3:0x36
	v_lshl_or_b32 v210, v40, 4, v38
	v_bitop3_b32 v40, v88, v39, 4 bitop3:0x36
	v_lshl_or_b32 v209, v40, 4, v38
	v_bitop3_b32 v39, v88, v39, 6 bitop3:0x36
	v_lshl_or_b32 v208, v39, 4, v38
	v_lshlrev_b32_e32 v201, 9, v88
	s_and_b32 s0, s16, 0x3fffffc0
	s_mov_b64 s[24:25], 0x6000
	s_lshl_b32 s38, s0, 2
	s_add_i32 s34, s36, 0x8000
	s_lshl_b32 s2, s2, 16
	s_lshl_b32 s3, s3, 18
	s_waitcnt vmcnt(3) lgkmcnt(0)
	v_mfma_f32_32x32x16_f16 v[18:33], v[34:37], v[154:157], v[2:17]
	ds_read_b128 v[34:37], v211 offset:4096
	s_and_b32 s2, s2, 0x200000
	s_lshl_b64 s[16:17], s[18:19], 22
	s_or_b32 s2, s2, s3
	s_or_b32 s16, s16, s2
	s_mov_b64 s[2:3], 0x1002000
	v_and_b32_e32 v90, 63, v0
	s_waitcnt lgkmcnt(0)
	v_mfma_f32_32x32x16_f16 v[2:17], v[34:37], v[154:157], v[2:17]
	ds_read_b128 v[34:37], v210
	s_mov_b32 s13, s19
	s_movk_i32 s42, 0x2000
	s_movk_i32 s39, 0x4000
	v_lshl_or_b32 v204, v191, 2, s38
	v_lshlrev_b32_e32 v212, 4, v88
	s_mov_b32 s40, -1
	s_waitcnt vmcnt(2) lgkmcnt(0)
	v_mfma_f32_32x32x16_f16 v[18:33], v[34:37], v[146:149], v[18:33]
	ds_read_b128 v[34:37], v210 offset:4096
	s_mov_b32 s41, 0x41000000
	s_mov_b32 s26, s19
	s_waitcnt lgkmcnt(0)
	v_mfma_f32_32x32x16_f16 v[2:17], v[34:37], v[146:149], v[2:17]
	ds_read_b128 v[34:37], v209
	s_waitcnt vmcnt(1) lgkmcnt(0)
	v_mfma_f32_32x32x16_f16 v[18:33], v[34:37], v[138:141], v[18:33]
	ds_read_b128 v[34:37], v209 offset:4096
	ds_read_b128 v[38:41], v208 offset:4096
	ds_read_b128 v[42:45], v208
	s_waitcnt lgkmcnt(2)
	v_mfma_f32_32x32x16_f16 v[2:17], v[34:37], v[138:141], v[2:17]
	v_lshlrev_b32_e32 v34, 5, v0
	v_lshlrev_b32_e32 v35, 1, v0
	v_lshlrev_b32_e32 v36, 3, v0
	v_and_b32_e32 v34, 0x180, v34
	v_and_b32_e32 v193, 24, v36
	v_and_or_b32 v34, v35, 32, v34
	v_or3_b32 v203, v34, v193, v201
	s_waitcnt vmcnt(0) lgkmcnt(0)
	v_mfma_f32_32x32x16_f16 v[18:33], v[42:45], v[134:137], v[18:33]
	v_and_b32_e32 v200, 64, v36
	v_bitop3_b32 v202, v36, 64, v36 bitop3:0xc
	v_or_b32_e32 v206, v203, v200
	v_or_b32_e32 v207, v203, v202
	v_mfma_f32_32x32x16_f16 v[2:17], v[38:41], v[134:137], v[2:17]
	s_nop 15
	s_nop 7
	s_nop 0
	v_max3_f32 v34, v18, v19, v2
	v_max3_f32 v35, v20, v21, v3
	s_nop 0
	v_max3_f32 v34, v34, v4, v5
	v_max3_f32 v35, v35, v24, v25
	s_nop 0
	v_max3_f32 v34, v34, v22, v23
	v_max3_f32 v35, v35, v8, v9
	s_nop 0
	v_max3_f32 v34, v34, v6, v7
	v_max3_f32 v35, v35, v28, v29
	s_nop 0
	v_max3_f32 v34, v34, v26, v27
	v_max3_f32 v35, v35, v12, v13
	s_nop 0
	v_max3_f32 v34, v34, v10, v11
	v_max3_f32 v35, v35, v32, v33
	s_nop 0
	v_max3_f32 v34, v34, v30, v31
	v_max3_f32 v35, v35, v16, v17
	s_nop 0
	v_max3_f32 v34, v34, v14, v15
	s_nop 0
	v_max_f32_e32 v34, v34, v35
	s_nop 0
	v_mov_b32_e32 v35, v34
	s_nop 1
	v_permlane32_swap_b32_e32 v34, v35
	v_max_f32_e32 v34, v34, v35
	s_nop 0
	v_add_f32_e32 v205, v183, v34
	v_sub_f32_e32 v18, v18, v34
	v_sub_f32_e32 v2, v2, v34
	v_sub_f32_e32 v19, v19, v34
	v_sub_f32_e32 v3, v3, v34
	v_sub_f32_e32 v20, v20, v34
	v_sub_f32_e32 v4, v4, v34
	v_sub_f32_e32 v21, v21, v34
	v_sub_f32_e32 v5, v5, v34
	v_sub_f32_e32 v22, v22, v34
	v_sub_f32_e32 v6, v6, v34
	v_sub_f32_e32 v23, v23, v34
	v_sub_f32_e32 v7, v7, v34
	v_sub_f32_e32 v24, v24, v34
	v_sub_f32_e32 v8, v8, v34
	v_sub_f32_e32 v25, v25, v34
	v_sub_f32_e32 v9, v9, v34
	v_sub_f32_e32 v26, v26, v34
	v_sub_f32_e32 v10, v10, v34
	v_sub_f32_e32 v27, v27, v34
	v_sub_f32_e32 v11, v11, v34
	v_sub_f32_e32 v28, v28, v34
	v_sub_f32_e32 v12, v12, v34
	v_sub_f32_e32 v29, v29, v34
	v_sub_f32_e32 v13, v13, v34
	v_sub_f32_e32 v30, v30, v34
	v_sub_f32_e32 v14, v14, v34
	v_sub_f32_e32 v31, v31, v34
	v_sub_f32_e32 v15, v15, v34
	v_sub_f32_e32 v32, v32, v34
	v_sub_f32_e32 v16, v16, v34
	v_sub_f32_e32 v33, v33, v34
	v_sub_f32_e32 v17, v17, v34
	s_nop 0
	v_xor_b32_e32 v34, 0x80000000, v205
	v_mov_b32_e32 v35, v34
	v_mov_b32_e32 v36, v34
	v_mov_b32_e32 v37, v34
	v_mov_b32_e32 v38, v34
	v_mov_b32_e32 v39, v34
	v_mov_b32_e32 v40, v34
	v_mov_b32_e32 v41, v34
	v_mov_b32_e32 v42, v34
	v_mov_b32_e32 v43, v34
	v_mov_b32_e32 v44, v34
	v_mov_b32_e32 v45, v34
	v_mov_b32_e32 v46, v34
	v_mov_b32_e32 v47, v34
	v_mov_b32_e32 v48, v34
	v_mov_b32_e32 v49, v34
	s_waitcnt vmcnt(0) lgkmcnt(0)
	s_barrier
	v_exp_f32_e32 v50, v2
	v_exp_f32_e32 v51, v3
	v_lshl_add_u64 v[2:3], v[186:187], 0, s[24:25]
	s_mov_b32 s0, m0
	s_mov_b32 m0, s36
	s_nop 0
	global_load_lds_dwordx4 v[2:3], off
	s_mov_b32 m0, s0
	v_lshl_add_u64 v[2:3], v[194:195], 0, s[20:21]
	s_mov_b32 s0, m0
	s_mov_b32 m0, s34
	s_nop 0
	global_load_lds_dwordx4 v[2:3], off
	s_mov_b32 m0, s0
	ds_read_b128 v[82:85], v211 offset:8192
	ds_read_b128 v[170:173], v211 offset:12288
	ds_read_b128 v[166:169], v210 offset:8192
	ds_read_b128 v[162:165], v210 offset:12288
	ds_read_b128 v[126:129], v209 offset:8192
	ds_read_b128 v[122:125], v209 offset:12288
	ds_read_b128 v[118:121], v208 offset:8192
	ds_read_b128 v[114:117], v208 offset:12288
	v_exp_f32_e32 v52, v4
	v_lshl_add_u64 v[2:3], s[16:17], 0, v[86:87]
	v_bitop3_b32 v4, v89, 7, v0 bitop3:0x48
	v_exp_f32_e32 v66, v18
	v_exp_f32_e32 v67, v19
	v_exp_f32_e32 v68, v20
	v_exp_f32_e32 v69, v21
	v_exp_f32_e32 v70, v22
	v_exp_f32_e32 v71, v23
	v_exp_f32_e32 v72, v24
	v_exp_f32_e32 v73, v25
	v_exp_f32_e32 v74, v26
	v_exp_f32_e32 v75, v27
	v_exp_f32_e32 v76, v28
	v_exp_f32_e32 v77, v29
	v_exp_f32_e32 v78, v30
	v_exp_f32_e32 v79, v31
	v_exp_f32_e32 v80, v32
	v_exp_f32_e32 v81, v33
	v_exp_f32_e32 v53, v5
	v_exp_f32_e32 v54, v6
	v_exp_f32_e32 v55, v7
	v_exp_f32_e32 v56, v8
	v_exp_f32_e32 v57, v9
	v_exp_f32_e32 v58, v10
	v_exp_f32_e32 v59, v11
	v_exp_f32_e32 v60, v12
	v_exp_f32_e32 v61, v13
	v_exp_f32_e32 v62, v14
	v_exp_f32_e32 v63, v15
	v_exp_f32_e32 v64, v16
	v_exp_f32_e32 v65, v17
	v_lshl_or_b32 v4, v4, 4, v2
	v_mov_b32_e32 v5, v3
	s_waitcnt vmcnt(2) lgkmcnt(0)
	s_barrier
	v_lshl_add_u64 v[4:5], s[4:5], 0, v[4:5]
	v_or_b32_e32 v2, v2, v182
	v_lshl_add_u64 v[188:189], v[4:5], 0, s[2:3]
	v_lshl_add_u64 v[2:3], s[4:5], 0, v[2:3]
	s_mov_b64 s[2:3], 0x2002000
	v_cmp_gt_u32_e64 s[0:1], 32, v90
	v_lshl_add_u64 v[196:197], v[2:3], 0, s[2:3]
	s_mov_b64 s[2:3], 0x8000
	v_mov_b32_e32 v2, v183
	v_mov_b32_e32 v3, v183
	v_mov_b32_e32 v4, v183
	v_mov_b32_e32 v5, v183
	v_mov_b32_e32 v6, v183
	v_mov_b32_e32 v7, v183
	v_mov_b32_e32 v8, v183
	v_mov_b32_e32 v9, v183
	v_mov_b32_e32 v10, v183
	v_mov_b32_e32 v11, v183
	v_mov_b32_e32 v12, v183
	v_mov_b32_e32 v13, v183
	v_mov_b32_e32 v14, v183
	v_mov_b32_e32 v15, v183
	v_mov_b32_e32 v16, v183
	v_mov_b32_e32 v17, v183
	v_mov_b32_e32 v18, v183
	v_mov_b32_e32 v19, v183
	v_mov_b32_e32 v20, v183
	v_mov_b32_e32 v21, v183
	v_mov_b32_e32 v22, v183
	v_mov_b32_e32 v23, v183
	v_mov_b32_e32 v24, v183
	v_mov_b32_e32 v25, v183
	v_mov_b32_e32 v26, v183
	v_mov_b32_e32 v27, v183
	v_mov_b32_e32 v28, v183
	v_mov_b32_e32 v29, v183
	v_mov_b32_e32 v30, v183
	v_mov_b32_e32 v31, v183
	v_mov_b32_e32 v32, v183
	v_mov_b32_e32 v33, v183
	v_subrev_u32_e32 v221, s14, v186
	v_subrev_u32_e32 v222, s10, v194
	s_add_u32 s50, s14, 0x8000
	s_addc_u32 s51, s15, 0
	s_add_u32 s52, s10, 0x4000
	s_addc_u32 s53, s11, 0
.Lu0_1:
	ds_read_b64_tr_b16 v[178:179], v206 offset:24576
	ds_read_b64_tr_b16 v[180:181], v206 offset:25600
	s_waitcnt lgkmcnt(9)
	v_mfma_f32_32x32x16_f16 v[98:113], v[82:85], v[154:157], v[34:49]
	v_add_f32_e32 v86, v66, v67
	v_add_f32_e32 v86, v68, v86
	v_add_f32_e32 v86, v69, v86
	v_add_f32_e32 v86, v70, v86
	v_add_f32_e32 v86, v71, v86
	v_cvt_pk_f16_f32 v158, v66, v67
	v_cvt_pk_f16_f32 v159, v68, v69
	ds_read_b64_tr_b16 v[174:175], v207 offset:24576
	ds_read_b64_tr_b16 v[176:177], v207 offset:25600
	v_add_f32_e32 v66, v72, v86
	s_waitcnt lgkmcnt(10)
	v_mfma_f32_32x32x16_f16 v[82:97], v[170:173], v[154:157], v[34:49]
	v_add_f32_e32 v66, v73, v66
	v_add_f32_e32 v66, v74, v66
	v_add_f32_e32 v66, v75, v66
	v_cvt_pk_f16_f32 v160, v70, v71
	v_cvt_pk_f16_f32 v161, v72, v73
	ds_read_b64_tr_b16 v[170:171], v206 offset:26624
	ds_read_b64_tr_b16 v[172:173], v206 offset:27648
	s_waitcnt lgkmcnt(11)
	v_mfma_f32_32x32x16_f16 v[98:113], v[166:169], v[146:149], v[98:113]
	v_add_f32_e32 v66, v76, v66
	v_add_f32_e32 v66, v77, v66
	v_add_f32_e32 v66, v78, v66
	v_add_f32_e32 v66, v79, v66
	v_cvt_pk_f16_f32 v150, v74, v75
	v_cvt_pk_f16_f32 v151, v76, v77
	ds_read_b64_tr_b16 v[74:75], v207 offset:26624
	ds_read_b64_tr_b16 v[76:77], v207 offset:27648
	s_waitcnt lgkmcnt(12)
	v_mfma_f32_32x32x16_f16 v[82:97], v[162:165], v[146:149], v[82:97]
	v_add_f32_e32 v66, v80, v66
	v_add_f32_e32 v66, v81, v66
	v_add_f32_e32 v66, v50, v66
	v_add_f32_e32 v66, v51, v66
	v_cvt_pk_f16_f32 v152, v78, v79
	v_cvt_pk_f16_f32 v153, v80, v81
	ds_read_b64_tr_b16 v[70:71], v206 offset:28672
	ds_read_b64_tr_b16 v[72:73], v206 offset:29696
	s_waitcnt lgkmcnt(13)
	v_mfma_f32_32x32x16_f16 v[98:113], v[126:129], v[138:141], v[98:113]
	v_add_f32_e32 v66, v52, v66
	v_add_f32_e32 v66, v53, v66
	v_add_f32_e32 v66, v54, v66
	v_add_f32_e32 v78, v55, v66
	v_cvt_pk_f16_f32 v142, v50, v51
	v_cvt_pk_f16_f32 v143, v52, v53
	ds_read_b64_tr_b16 v[66:67], v207 offset:28672
	ds_read_b64_tr_b16 v[68:69], v207 offset:29696
	s_waitcnt lgkmcnt(14)
	v_mfma_f32_32x32x16_f16 v[82:97], v[122:125], v[138:141], v[82:97]
	v_add_f32_e32 v50, v56, v78
	v_add_f32_e32 v50, v57, v50
	v_add_f32_e32 v50, v58, v50
	v_add_f32_e32 v50, v59, v50
	v_cvt_pk_f16_f32 v144, v54, v55
	v_cvt_pk_f16_f32 v145, v56, v57
	ds_read_b64_tr_b16 v[54:55], v206 offset:30720
	ds_read_b64_tr_b16 v[56:57], v206 offset:31744
	s_waitcnt lgkmcnt(14)
	v_mfma_f32_32x32x16_f16 v[98:113], v[118:121], v[134:137], v[98:113]
	v_add_f32_e32 v50, v60, v50
	v_add_f32_e32 v50, v61, v50
	v_add_f32_e32 v50, v62, v50
	v_add_f32_e32 v78, v63, v50
	v_cvt_pk_f16_f32 v130, v58, v59
	v_cvt_pk_f16_f32 v131, v60, v61
	ds_read_b64_tr_b16 v[50:51], v207 offset:30720
	ds_read_b64_tr_b16 v[52:53], v207 offset:31744
	v_mfma_f32_32x32x16_f16 v[82:97], v[114:117], v[134:137], v[82:97]
	v_add_f32_e32 v58, v64, v78
	v_add_f32_e32 v60, v65, v58
	v_cvt_pk_f16_f32 v132, v62, v63
	v_cvt_pk_f16_f32 v133, v64, v65
	s_cmp_lg_u32 s47, 0
	s_cbranch_scc1 .Ldh1_skip
	s_add_i32 s26, s42, s36
	s_mov_b32 m0, s26
	s_nop 0
	global_load_lds_dwordx4 v221, s[50:51]
	s_add_u32 s56, s50, 0x1000
	s_addc_u32 s57, s51, 0
	s_add_i32 s26, s26, 0x1000
	s_mov_b32 m0, s26
	s_nop 0
	global_load_lds_dwordx4 v221, s[56:57]
	s_add_i32 s26, s39, s35
	s_mov_b32 m0, s26
	s_nop 0
	global_load_lds_dwordx4 v222, s[52:53]
	s_add_u32 s56, s52, 0x1000
	s_addc_u32 s57, s53, 0
	s_add_i32 s26, s26, 0x1000
	s_mov_b32 m0, s26
	s_nop 0
	global_load_lds_dwordx4 v222, s[56:57]
.Ldh1_join:
	v_max_f32_e32 v58, v98, v99
	v_max3_f32 v59, v100, v101, v83
	v_max3_f32 v58, v58, v82, v84
	v_max3_f32 v58, v58, v85, v102
	v_max3_f32 v59, v59, v104, v105
	v_max3_f32 v58, v58, v103, v86
	v_max3_f32 v59, v59, v88, v89
	v_max3_f32 v58, v58, v87, v106
	v_max3_f32 v59, v59, v108, v109
	v_max3_f32 v58, v58, v107, v90
	v_max3_f32 v59, v59, v92, v93
	v_max3_f32 v58, v58, v91, v110
	v_max3_f32 v59, v59, v112, v113
	v_max3_f32 v58, v58, v111, v94
	v_max3_f32 v59, v59, v96, v97
	v_max3_f32 v58, v58, v95, v59
	v_add_f32_e32 v198, v183, v60
	v_cmp_lt_f32_e32 vcc, s41, v58
	s_cmp_lg_u64 vcc, 0
	s_cselect_b64 s[26:27], -1, 0
	s_cbranch_vccnz .Lu0_9
.Lu0_2:
	s_waitcnt lgkmcnt(14)
	v_mfma_f32_32x32x16_f16 v[2:17], v[158:161], v[178:181], v[2:17]
	v_exp_f32_e32 v98, v98
	v_exp_f32_e32 v99, v99
	v_exp_f32_e32 v100, v100
	v_exp_f32_e32 v101, v101
	s_waitcnt lgkmcnt(12)
	v_mfma_f32_32x32x16_f16 v[18:33], v[158:161], v[174:177], v[18:33]
	v_exp_f32_e32 v102, v102
	v_exp_f32_e32 v103, v103
	v_exp_f32_e32 v104, v104
	v_exp_f32_e32 v105, v105
	ds_read_b128 v[58:61], v211 offset:16384
	ds_read_b128 v[114:117], v211 offset:20480
	s_waitcnt lgkmcnt(12)
	v_mfma_f32_32x32x16_f16 v[2:17], v[150:153], v[170:173], v[2:17]
	v_exp_f32_e32 v106, v106
	v_exp_f32_e32 v107, v107
	v_exp_f32_e32 v108, v108
	v_exp_f32_e32 v109, v109
	ds_read_b128 v[182:185], v210 offset:16384
	ds_read_b128 v[174:177], v210 offset:20480
	s_waitcnt lgkmcnt(12)
	v_mfma_f32_32x32x16_f16 v[18:33], v[150:153], v[74:77], v[18:33]
	v_exp_f32_e32 v110, v110
	v_exp_f32_e32 v111, v111
	v_exp_f32_e32 v112, v112
	v_exp_f32_e32 v113, v113
	ds_read_b128 v[178:181], v209 offset:16384
	ds_read_b128 v[166:169], v209 offset:20480
	s_waitcnt lgkmcnt(12)
	v_mfma_f32_32x32x16_f16 v[2:17], v[142:145], v[70:73], v[2:17]
	v_exp_f32_e32 v82, v82
	v_exp_f32_e32 v83, v83
	v_exp_f32_e32 v84, v84
	v_exp_f32_e32 v85, v85
	ds_read_b128 v[170:173], v208 offset:16384
	ds_read_b128 v[162:165], v208 offset:20480
	s_waitcnt lgkmcnt(12)
	v_mfma_f32_32x32x16_f16 v[18:33], v[142:145], v[66:69], v[18:33]
	v_exp_f32_e32 v86, v86
	v_exp_f32_e32 v87, v87
	v_exp_f32_e32 v88, v88
	v_exp_f32_e32 v89, v89
	s_waitcnt lgkmcnt(10)
	v_mfma_f32_32x32x16_f16 v[2:17], v[130:133], v[54:57], v[2:17]
	v_exp_f32_e32 v90, v90
	v_exp_f32_e32 v91, v91
	v_exp_f32_e32 v92, v92
	v_exp_f32_e32 v93, v93
	s_waitcnt lgkmcnt(8)
	v_mfma_f32_32x32x16_f16 v[18:33], v[130:133], v[50:53], v[18:33]
	v_exp_f32_e32 v94, v94
	v_exp_f32_e32 v95, v95
	v_exp_f32_e32 v96, v96
	v_exp_f32_e32 v97, v97
	s_cmp_lg_u32 s47, 0
	s_cbranch_scc1 .Ldw1_o
	s_waitcnt vmcnt(4) lgkmcnt(0)
	s_branch .Ldw1_j
.Ldw1_o:
	s_waitcnt vmcnt(0) lgkmcnt(0)
.Ldw1_j:
	s_barrier
	s_andn2_b64 vcc, exec, s[26:27]
	s_cbranch_vccnz .Lu0_4
	s_waitcnt lgkmcnt(0)
	v_add_u32_e32 v66, s38, v212
	ds_read_b128 v[50:53], v66 offset:49248
	ds_read_b128 v[54:57], v66 offset:49216
	ds_read_b128 v[62:65], v66 offset:49184
	ds_read_b128 v[66:69], v66 offset:49152
	s_waitcnt lgkmcnt(3)
	v_pk_mul_f32 v[14:15], v[14:15], v[50:51]
	s_waitcnt lgkmcnt(2)
	v_pk_mul_f32 v[10:11], v[10:11], v[54:55]
	s_waitcnt lgkmcnt(1)
	v_pk_mul_f32 v[6:7], v[6:7], v[62:63]
	v_pk_mul_f32 v[16:17], v[16:17], v[52:53]
	v_pk_mul_f32 v[12:13], v[12:13], v[56:57]
	v_pk_mul_f32 v[8:9], v[8:9], v[64:65]
	s_waitcnt lgkmcnt(0)
	v_pk_mul_f32 v[4:5], v[4:5], v[68:69]
	v_pk_mul_f32 v[2:3], v[2:3], v[66:67]
	v_pk_mul_f32 v[30:31], v[30:31], v[50:51]
	v_pk_mul_f32 v[26:27], v[26:27], v[54:55]
	v_pk_mul_f32 v[22:23], v[22:23], v[62:63]
	v_pk_mul_f32 v[32:33], v[32:33], v[52:53]
	v_pk_mul_f32 v[28:29], v[28:29], v[56:57]
	v_pk_mul_f32 v[24:25], v[24:25], v[64:65]
	v_pk_mul_f32 v[20:21], v[20:21], v[68:69]
	v_pk_mul_f32 v[18:19], v[18:19], v[66:67]
.Lu0_4:
	s_add_i32 s26, s39, 0x2000
	s_cmpk_lg_i32 s39, 0x4000
	s_cselect_b32 s43, s26, 0
	ds_read_b64_tr_b16 v[126:127], v206 offset:32768
	ds_read_b64_tr_b16 v[128:129], v206 offset:33792
	s_waitcnt lgkmcnt(9)
	v_mfma_f32_32x32x16_f16 v[66:81], v[58:61], v[154:157], v[34:49]
	v_add_f32_e32 v50, v98, v99
	v_add_f32_e32 v50, v100, v50
	v_add_f32_e32 v50, v101, v50
	v_add_f32_e32 v50, v102, v50
	v_add_f32_e32 v50, v103, v50
	v_cvt_pk_f16_f32 v158, v98, v99
	v_cvt_pk_f16_f32 v159, v100, v101
	ds_read_b64_tr_b16 v[122:123], v207 offset:32768
	ds_read_b64_tr_b16 v[124:125], v207 offset:33792
	v_add_f32_e32 v50, v104, v50
	v_add_f32_e32 v50, v105, v50
	v_add_f32_e32 v50, v106, v50
	v_add_f32_e32 v98, v107, v50
	s_waitcnt lgkmcnt(10)
	v_mfma_f32_32x32x16_f16 v[50:65], v[114:117], v[154:157], v[34:49]
	v_cvt_pk_f16_f32 v160, v102, v103
	v_cvt_pk_f16_f32 v161, v104, v105
	ds_read_b64_tr_b16 v[118:119], v206 offset:34816
	ds_read_b64_tr_b16 v[120:121], v206 offset:35840
	s_waitcnt lgkmcnt(11)
	v_mfma_f32_32x32x16_f16 v[66:81], v[182:185], v[146:149], v[66:81]
	v_add_f32_e32 v98, v108, v98
	v_add_f32_e32 v98, v109, v98
	v_add_f32_e32 v98, v110, v98
	v_add_f32_e32 v98, v111, v98
	v_cvt_pk_f16_f32 v150, v106, v107
	v_cvt_pk_f16_f32 v151, v108, v109
	ds_read_b64_tr_b16 v[114:115], v207 offset:34816
	ds_read_b64_tr_b16 v[116:117], v207 offset:35840
	s_waitcnt lgkmcnt(12)
	v_mfma_f32_32x32x16_f16 v[50:65], v[174:177], v[146:149], v[50:65]
	v_add_f32_e32 v98, v112, v98
	v_add_f32_e32 v98, v113, v98
	v_add_f32_e32 v98, v82, v98
	v_add_f32_e32 v98, v83, v98
	v_cvt_pk_f16_f32 v152, v110, v111
	v_cvt_pk_f16_f32 v153, v112, v113
	ds_read_b64_tr_b16 v[106:107], v206 offset:36864
	ds_read_b64_tr_b16 v[108:109], v206 offset:37888
	s_waitcnt lgkmcnt(13)
	v_mfma_f32_32x32x16_f16 v[66:81], v[178:181], v[138:141], v[66:81]
	v_add_f32_e32 v98, v84, v98
	v_add_f32_e32 v98, v85, v98
	v_add_f32_e32 v98, v86, v98
	v_add_f32_e32 v98, v87, v98
	v_cvt_pk_f16_f32 v142, v82, v83
	v_cvt_pk_f16_f32 v143, v84, v85
	ds_read_b64_tr_b16 v[102:103], v207 offset:36864
	ds_read_b64_tr_b16 v[104:105], v207 offset:37888
	s_waitcnt lgkmcnt(14)
	v_mfma_f32_32x32x16_f16 v[50:65], v[166:169], v[138:141], v[50:65]
	v_add_f32_e32 v82, v88, v98
	v_add_f32_e32 v82, v89, v82
	v_add_f32_e32 v82, v90, v82
	v_add_f32_e32 v82, v91, v82
	v_cvt_pk_f16_f32 v144, v86, v87
	v_cvt_pk_f16_f32 v145, v88, v89
	ds_read_b64_tr_b16 v[98:99], v206 offset:38912
	ds_read_b64_tr_b16 v[100:101], v206 offset:39936
	s_waitcnt lgkmcnt(14)
	v_mfma_f32_32x32x16_f16 v[66:81], v[170:173], v[134:137], v[66:81]
	v_add_f32_e32 v82, v92, v82
	v_add_f32_e32 v82, v93, v82
	v_add_f32_e32 v82, v94, v82
	v_add_f32_e32 v82, v95, v82
	v_cvt_pk_f16_f32 v130, v90, v91
	v_cvt_pk_f16_f32 v131, v92, v93
	ds_read_b64_tr_b16 v[86:87], v207 offset:38912
	ds_read_b64_tr_b16 v[88:89], v207 offset:39936
	v_mfma_f32_32x32x16_f16 v[50:65], v[162:165], v[134:137], v[50:65]
	v_add_f32_e32 v82, v96, v82
	v_add_f32_e32 v84, v97, v82
	v_cvt_pk_f16_f32 v132, v94, v95
	v_cvt_pk_f16_f32 v133, v96, v97
	s_cmp_lg_u32 s47, 0
	s_cbranch_scc1 .Ldh2_skip
	s_add_u32 s54, s50, 0x2000
	s_addc_u32 s55, s51, 0
	s_add_i32 s26, s39, s36
	s_mov_b32 m0, s26
	s_nop 0
	global_load_lds_dwordx4 v221, s[54:55]
	s_add_u32 s56, s54, 0x1000
	s_addc_u32 s57, s55, 0
	s_add_i32 s26, s26, 0x1000
	s_mov_b32 m0, s26
	s_nop 0
	global_load_lds_dwordx4 v221, s[56:57]
.Ldh2_join:
	v_max_f32_e32 v82, v66, v67
	s_nop 1
	v_max3_f32 v83, v68, v69, v51
	v_max3_f32 v82, v82, v50, v52
	v_max3_f32 v82, v82, v53, v70
	v_max3_f32 v83, v83, v72, v73
	v_max3_f32 v82, v82, v71, v54
	v_max3_f32 v83, v83, v56, v57
	v_max3_f32 v82, v82, v55, v74
	v_max3_f32 v83, v83, v76, v77
	v_max3_f32 v82, v82, v75, v58
	v_max3_f32 v83, v83, v60, v61
	v_max3_f32 v82, v82, v59, v78
	v_max3_f32 v83, v83, v80, v81
	v_max3_f32 v82, v82, v79, v62
	v_max3_f32 v83, v83, v64, v65
	v_max3_f32 v82, v82, v63, v83
	v_add_f32_e32 v183, v198, v84
	s_cmp_lg_u32 s47, 0
	s_cbranch_scc1 .Ldh3_skip
	s_add_u32 s54, s52, 0x2000
	s_addc_u32 s55, s53, 0
	s_add_i32 s26, s43, s35
	s_mov_b32 m0, s26
	s_nop 0
	global_load_lds_dwordx4 v222, s[54:55]
	s_add_u32 s56, s54, 0x1000
	s_addc_u32 s57, s55, 0
	s_add_i32 s26, s26, 0x1000
	s_mov_b32 m0, s26
	s_nop 0
	global_load_lds_dwordx4 v222, s[56:57]
.Ldh3_join:
	v_cmp_lt_f32_e32 vcc, s41, v82
	s_cmp_lg_u64 vcc, 0
	s_cselect_b64 s[26:27], -1, 0
	s_cbranch_vccnz .Lu0_12
.Lu0_5:
	s_waitcnt lgkmcnt(14)
	v_mfma_f32_32x32x16_f16 v[2:17], v[158:161], v[126:129], v[2:17]
	v_exp_f32_e32 v66, v66
	v_exp_f32_e32 v67, v67
	v_exp_f32_e32 v68, v68
	v_exp_f32_e32 v69, v69
	s_waitcnt lgkmcnt(12)
	v_mfma_f32_32x32x16_f16 v[18:33], v[158:161], v[122:125], v[18:33]
	v_exp_f32_e32 v70, v70
	v_exp_f32_e32 v71, v71
	v_exp_f32_e32 v72, v72
	v_exp_f32_e32 v73, v73
	ds_read_b128 v[82:85], v211
	ds_read_b128 v[170:173], v211 offset:4096
	s_waitcnt lgkmcnt(12)
	v_mfma_f32_32x32x16_f16 v[2:17], v[150:153], v[118:121], v[2:17]
	v_exp_f32_e32 v74, v74
	v_exp_f32_e32 v75, v75
	v_exp_f32_e32 v76, v76
	v_exp_f32_e32 v77, v77
	ds_read_b128 v[166:169], v210
	ds_read_b128 v[162:165], v210 offset:4096
	s_waitcnt lgkmcnt(12)
	v_mfma_f32_32x32x16_f16 v[18:33], v[150:153], v[114:117], v[18:33]
	v_exp_f32_e32 v78, v78
	v_exp_f32_e32 v79, v79
	v_exp_f32_e32 v80, v80
	v_exp_f32_e32 v81, v81
	ds_read_b128 v[126:129], v209
	ds_read_b128 v[122:125], v209 offset:4096
	s_waitcnt lgkmcnt(12)
	v_mfma_f32_32x32x16_f16 v[2:17], v[142:145], v[106:109], v[2:17]
	v_exp_f32_e32 v50, v50
	v_exp_f32_e32 v51, v51
	v_exp_f32_e32 v52, v52
	v_exp_f32_e32 v53, v53
	ds_read_b128 v[118:121], v208
	ds_read_b128 v[114:117], v208 offset:4096
	s_waitcnt lgkmcnt(12)
	v_mfma_f32_32x32x16_f16 v[18:33], v[142:145], v[102:105], v[18:33]
	v_exp_f32_e32 v54, v54
	v_exp_f32_e32 v55, v55
	v_exp_f32_e32 v56, v56
	v_exp_f32_e32 v57, v57
	s_waitcnt lgkmcnt(10)
	v_mfma_f32_32x32x16_f16 v[2:17], v[130:133], v[98:101], v[2:17]
	v_exp_f32_e32 v58, v58
	v_exp_f32_e32 v59, v59
	v_exp_f32_e32 v60, v60
	v_exp_f32_e32 v61, v61
	s_waitcnt lgkmcnt(8)
	v_mfma_f32_32x32x16_f16 v[18:33], v[130:133], v[86:89], v[18:33]
	v_exp_f32_e32 v62, v62
	v_exp_f32_e32 v63, v63
	v_exp_f32_e32 v64, v64
	v_exp_f32_e32 v65, v65
	s_cmp_lg_u32 s47, 0
	s_cbranch_scc1 .Ldw2_o
	s_waitcnt vmcnt(4) lgkmcnt(0)
	s_branch .Ldw2_j

.Ldw2_j:
	s_barrier
	s_andn2_b64 vcc, exec, s[26:27]
	s_cbranch_vccnz .Lu0_7
	s_waitcnt lgkmcnt(0)
	v_add_u32_e32 v98, s38, v212
	ds_read_b128 v[86:89], v98 offset:49248
	ds_read_b128 v[90:93], v98 offset:49216
	ds_read_b128 v[94:97], v98 offset:49152
	ds_read_b128 v[98:101], v98 offset:49184
	s_waitcnt lgkmcnt(3)
	v_pk_mul_f32 v[16:17], v[16:17], v[88:89]
	v_pk_mul_f32 v[14:15], v[14:15], v[86:87]
	s_waitcnt lgkmcnt(2)
	v_pk_mul_f32 v[12:13], v[12:13], v[92:93]
	v_pk_mul_f32 v[10:11], v[10:11], v[90:91]
	s_waitcnt lgkmcnt(0)
	v_pk_mul_f32 v[8:9], v[8:9], v[100:101]
	v_pk_mul_f32 v[6:7], v[6:7], v[98:99]
	v_pk_mul_f32 v[4:5], v[4:5], v[96:97]
	v_pk_mul_f32 v[2:3], v[2:3], v[94:95]
	v_pk_mul_f32 v[32:33], v[32:33], v[88:89]
	v_pk_mul_f32 v[30:31], v[30:31], v[86:87]
	v_pk_mul_f32 v[28:29], v[28:29], v[92:93]
	v_pk_mul_f32 v[26:27], v[26:27], v[90:91]
	v_pk_mul_f32 v[24:25], v[24:25], v[100:101]
	v_pk_mul_f32 v[22:23], v[22:23], v[98:99]
	v_pk_mul_f32 v[20:21], v[20:21], v[96:97]
	v_pk_mul_f32 v[18:19], v[18:19], v[94:95]

.Lu1_1:
	ds_read_b64_tr_b16 v[178:179], v206 offset:40960
	ds_read_b64_tr_b16 v[180:181], v206 offset:41984
	s_waitcnt lgkmcnt(9)
	v_mfma_f32_32x32x16_f16 v[98:113], v[82:85], v[154:157], v[34:49]
	v_add_f32_e32 v86, v66, v67
	v_add_f32_e32 v86, v68, v86
	v_add_f32_e32 v86, v69, v86
	v_add_f32_e32 v86, v70, v86
	v_add_f32_e32 v86, v71, v86
	v_cvt_pk_f16_f32 v158, v66, v67
	v_cvt_pk_f16_f32 v159, v68, v69
	ds_read_b64_tr_b16 v[174:175], v207 offset:40960
	ds_read_b64_tr_b16 v[176:177], v207 offset:41984
	v_add_f32_e32 v66, v72, v86
	s_waitcnt lgkmcnt(10)
	v_mfma_f32_32x32x16_f16 v[82:97], v[170:173], v[154:157], v[34:49]
	v_add_f32_e32 v66, v73, v66
	v_add_f32_e32 v66, v74, v66
	v_add_f32_e32 v66, v75, v66
	v_cvt_pk_f16_f32 v160, v70, v71
	v_cvt_pk_f16_f32 v161, v72, v73
	ds_read_b64_tr_b16 v[170:171], v206 offset:43008
	ds_read_b64_tr_b16 v[172:173], v206 offset:44032
	s_waitcnt lgkmcnt(11)
	v_mfma_f32_32x32x16_f16 v[98:113], v[166:169], v[146:149], v[98:113]
	v_add_f32_e32 v66, v76, v66
	v_add_f32_e32 v66, v77, v66
	v_add_f32_e32 v66, v78, v66
	v_add_f32_e32 v66, v79, v66
	v_cvt_pk_f16_f32 v150, v74, v75
	v_cvt_pk_f16_f32 v151, v76, v77
	ds_read_b64_tr_b16 v[74:75], v207 offset:43008
	ds_read_b64_tr_b16 v[76:77], v207 offset:44032
	s_waitcnt lgkmcnt(12)
	v_mfma_f32_32x32x16_f16 v[82:97], v[162:165], v[146:149], v[82:97]
	v_add_f32_e32 v66, v80, v66
	v_add_f32_e32 v66, v81, v66
	v_add_f32_e32 v66, v50, v66
	v_add_f32_e32 v66, v51, v66
	v_cvt_pk_f16_f32 v152, v78, v79
	v_cvt_pk_f16_f32 v153, v80, v81
	ds_read_b64_tr_b16 v[70:71], v206 offset:45056
	ds_read_b64_tr_b16 v[72:73], v206 offset:46080
	s_waitcnt lgkmcnt(13)
	v_mfma_f32_32x32x16_f16 v[98:113], v[126:129], v[138:141], v[98:113]
	v_add_f32_e32 v66, v52, v66
	v_add_f32_e32 v66, v53, v66
	v_add_f32_e32 v66, v54, v66
	v_add_f32_e32 v78, v55, v66
	v_cvt_pk_f16_f32 v142, v50, v51
	v_cvt_pk_f16_f32 v143, v52, v53
	ds_read_b64_tr_b16 v[66:67], v207 offset:45056
	ds_read_b64_tr_b16 v[68:69], v207 offset:46080
	s_waitcnt lgkmcnt(14)
	v_mfma_f32_32x32x16_f16 v[82:97], v[122:125], v[138:141], v[82:97]
	v_add_f32_e32 v50, v56, v78
	v_add_f32_e32 v50, v57, v50
	v_add_f32_e32 v50, v58, v50
	v_add_f32_e32 v50, v59, v50
	v_cvt_pk_f16_f32 v144, v54, v55
	v_cvt_pk_f16_f32 v145, v56, v57
	ds_read_b64_tr_b16 v[54:55], v206 offset:47104
	ds_read_b64_tr_b16 v[56:57], v206 offset:48128
	s_waitcnt lgkmcnt(14)
	v_mfma_f32_32x32x16_f16 v[98:113], v[118:121], v[134:137], v[98:113]
	v_add_f32_e32 v50, v60, v50
	v_add_f32_e32 v50, v61, v50
	v_add_f32_e32 v50, v62, v50
	v_add_f32_e32 v78, v63, v50
	v_cvt_pk_f16_f32 v130, v58, v59
	v_cvt_pk_f16_f32 v131, v60, v61
	ds_read_b64_tr_b16 v[50:51], v207 offset:47104
	ds_read_b64_tr_b16 v[52:53], v207 offset:48128
	v_mfma_f32_32x32x16_f16 v[82:97], v[114:117], v[134:137], v[82:97]
	v_add_f32_e32 v58, v64, v78
	v_add_f32_e32 v60, v65, v58
	v_cvt_pk_f16_f32 v132, v62, v63
	v_cvt_pk_f16_f32 v133, v64, v65
	s_cmp_lg_u32 s47, 0
	s_cbranch_scc1 .Ldh4_skip
	s_add_i32 s26, s42, s36
	s_mov_b32 m0, s26
	s_nop 0
	global_load_lds_dwordx4 v221, s[50:51]
	s_add_u32 s56, s50, 0x1000
	s_addc_u32 s57, s51, 0
	s_add_i32 s26, s26, 0x1000
	s_mov_b32 m0, s26
	s_nop 0
	global_load_lds_dwordx4 v221, s[56:57]
	s_add_i32 s26, s39, s35
	s_mov_b32 m0, s26
	s_nop 0
	global_load_lds_dwordx4 v222, s[52:53]
	s_add_u32 s56, s52, 0x1000
	s_addc_u32 s57, s53, 0
	s_add_i32 s26, s26, 0x1000
	s_mov_b32 m0, s26
	s_nop 0
	global_load_lds_dwordx4 v222, s[56:57]

.Lu1_2:
	s_waitcnt lgkmcnt(14)
	v_mfma_f32_32x32x16_f16 v[2:17], v[158:161], v[178:181], v[2:17]
	v_exp_f32_e32 v98, v98
	v_exp_f32_e32 v99, v99
	v_exp_f32_e32 v100, v100
	v_exp_f32_e32 v101, v101
	s_waitcnt lgkmcnt(12)
	v_mfma_f32_32x32x16_f16 v[18:33], v[158:161], v[174:177], v[18:33]
	v_exp_f32_e32 v102, v102
	v_exp_f32_e32 v103, v103
	v_exp_f32_e32 v104, v104
	v_exp_f32_e32 v105, v105
	ds_read_b128 v[58:61], v211 offset:8192
	ds_read_b128 v[114:117], v211 offset:12288
	s_waitcnt lgkmcnt(12)
	v_mfma_f32_32x32x16_f16 v[2:17], v[150:153], v[170:173], v[2:17]
	v_exp_f32_e32 v106, v106
	v_exp_f32_e32 v107, v107
	v_exp_f32_e32 v108, v108
	v_exp_f32_e32 v109, v109
	ds_read_b128 v[182:185], v210 offset:8192
	ds_read_b128 v[174:177], v210 offset:12288
	s_waitcnt lgkmcnt(12)
	v_mfma_f32_32x32x16_f16 v[18:33], v[150:153], v[74:77], v[18:33]
	v_exp_f32_e32 v110, v110
	v_exp_f32_e32 v111, v111
	v_exp_f32_e32 v112, v112
	v_exp_f32_e32 v113, v113
	ds_read_b128 v[178:181], v209 offset:8192
	ds_read_b128 v[166:169], v209 offset:12288
	s_waitcnt lgkmcnt(12)
	v_mfma_f32_32x32x16_f16 v[2:17], v[142:145], v[70:73], v[2:17]
	v_exp_f32_e32 v82, v82
	v_exp_f32_e32 v83, v83
	v_exp_f32_e32 v84, v84
	v_exp_f32_e32 v85, v85
	ds_read_b128 v[170:173], v208 offset:8192
	ds_read_b128 v[162:165], v208 offset:12288
	s_waitcnt lgkmcnt(12)
	v_mfma_f32_32x32x16_f16 v[18:33], v[142:145], v[66:69], v[18:33]
	v_exp_f32_e32 v86, v86
	v_exp_f32_e32 v87, v87
	v_exp_f32_e32 v88, v88
	v_exp_f32_e32 v89, v89
	s_waitcnt lgkmcnt(10)
	v_mfma_f32_32x32x16_f16 v[2:17], v[130:133], v[54:57], v[2:17]
	v_exp_f32_e32 v90, v90
	v_exp_f32_e32 v91, v91
	v_exp_f32_e32 v92, v92
	v_exp_f32_e32 v93, v93
	s_waitcnt lgkmcnt(8)
	v_mfma_f32_32x32x16_f16 v[18:33], v[130:133], v[50:53], v[18:33]
	v_exp_f32_e32 v94, v94
	v_exp_f32_e32 v95, v95
	v_exp_f32_e32 v96, v96
	v_exp_f32_e32 v97, v97
	s_cmp_lg_u32 s47, 0
	s_cbranch_scc1 .Ldw3_o
	s_waitcnt vmcnt(4) lgkmcnt(0)
	s_branch .Ldw3_j

.Lu1_4:
	s_add_i32 s26, s39, 0x2000
	s_cmpk_lg_i32 s39, 0x4000
	s_cselect_b32 s43, s26, 0
	ds_read_b64_tr_b16 v[126:127], v206 offset:24576
	ds_read_b64_tr_b16 v[128:129], v206 offset:25600
	s_waitcnt lgkmcnt(9)
	v_mfma_f32_32x32x16_f16 v[66:81], v[58:61], v[154:157], v[34:49]
	v_add_f32_e32 v50, v98, v99
	v_add_f32_e32 v50, v100, v50
	v_add_f32_e32 v50, v101, v50
	v_add_f32_e32 v50, v102, v50
	v_add_f32_e32 v50, v103, v50
	v_cvt_pk_f16_f32 v158, v98, v99
	v_cvt_pk_f16_f32 v159, v100, v101
	ds_read_b64_tr_b16 v[122:123], v207 offset:24576
	ds_read_b64_tr_b16 v[124:125], v207 offset:25600
	v_add_f32_e32 v50, v104, v50
	v_add_f32_e32 v50, v105, v50
	v_add_f32_e32 v50, v106, v50
	v_add_f32_e32 v98, v107, v50
	s_waitcnt lgkmcnt(10)
	v_mfma_f32_32x32x16_f16 v[50:65], v[114:117], v[154:157], v[34:49]
	v_cvt_pk_f16_f32 v160, v102, v103
	v_cvt_pk_f16_f32 v161, v104, v105
	ds_read_b64_tr_b16 v[118:119], v206 offset:26624
	ds_read_b64_tr_b16 v[120:121], v206 offset:27648
	s_waitcnt lgkmcnt(11)
	v_mfma_f32_32x32x16_f16 v[66:81], v[182:185], v[146:149], v[66:81]
	v_add_f32_e32 v98, v108, v98
	v_add_f32_e32 v98, v109, v98
	v_add_f32_e32 v98, v110, v98
	v_add_f32_e32 v98, v111, v98
	v_cvt_pk_f16_f32 v150, v106, v107
	v_cvt_pk_f16_f32 v151, v108, v109
	ds_read_b64_tr_b16 v[114:115], v207 offset:26624
	ds_read_b64_tr_b16 v[116:117], v207 offset:27648
	s_waitcnt lgkmcnt(12)
	v_mfma_f32_32x32x16_f16 v[50:65], v[174:177], v[146:149], v[50:65]
	v_add_f32_e32 v98, v112, v98
	v_add_f32_e32 v98, v113, v98
	v_add_f32_e32 v98, v82, v98
	v_add_f32_e32 v98, v83, v98
	v_cvt_pk_f16_f32 v152, v110, v111
	v_cvt_pk_f16_f32 v153, v112, v113
	ds_read_b64_tr_b16 v[106:107], v206 offset:28672
	ds_read_b64_tr_b16 v[108:109], v206 offset:29696
	s_waitcnt lgkmcnt(13)
	v_mfma_f32_32x32x16_f16 v[66:81], v[178:181], v[138:141], v[66:81]
	v_add_f32_e32 v98, v84, v98
	v_add_f32_e32 v98, v85, v98
	v_add_f32_e32 v98, v86, v98
	v_add_f32_e32 v98, v87, v98
	v_cvt_pk_f16_f32 v142, v82, v83
	v_cvt_pk_f16_f32 v143, v84, v85
	ds_read_b64_tr_b16 v[102:103], v207 offset:28672
	ds_read_b64_tr_b16 v[104:105], v207 offset:29696
	s_waitcnt lgkmcnt(14)
	v_mfma_f32_32x32x16_f16 v[50:65], v[166:169], v[138:141], v[50:65]
	v_add_f32_e32 v82, v88, v98
	v_add_f32_e32 v82, v89, v82
	v_add_f32_e32 v82, v90, v82
	v_add_f32_e32 v82, v91, v82
	v_cvt_pk_f16_f32 v144, v86, v87
	v_cvt_pk_f16_f32 v145, v88, v89
	ds_read_b64_tr_b16 v[98:99], v206 offset:30720
	ds_read_b64_tr_b16 v[100:101], v206 offset:31744
	s_waitcnt lgkmcnt(14)
	v_mfma_f32_32x32x16_f16 v[66:81], v[170:173], v[134:137], v[66:81]
	v_add_f32_e32 v82, v92, v82
	v_add_f32_e32 v82, v93, v82
	v_add_f32_e32 v82, v94, v82
	v_add_f32_e32 v82, v95, v82
	v_cvt_pk_f16_f32 v130, v90, v91
	v_cvt_pk_f16_f32 v131, v92, v93
	ds_read_b64_tr_b16 v[86:87], v207 offset:30720
	ds_read_b64_tr_b16 v[88:89], v207 offset:31744
	v_mfma_f32_32x32x16_f16 v[50:65], v[162:165], v[134:137], v[50:65]
	v_add_f32_e32 v82, v96, v82
	v_add_f32_e32 v84, v97, v82
	v_cvt_pk_f16_f32 v132, v94, v95
	v_cvt_pk_f16_f32 v133, v96, v97
	s_cmp_lg_u32 s47, 0
	s_cbranch_scc1 .Ldh5_skip
	s_add_u32 s54, s50, 0x2000
	s_addc_u32 s55, s51, 0
	s_add_i32 s26, s39, s36
	s_mov_b32 m0, s26
	s_nop 0
	global_load_lds_dwordx4 v221, s[54:55]
	s_add_u32 s56, s54, 0x1000
	s_addc_u32 s57, s55, 0
	s_add_i32 s26, s26, 0x1000
	s_mov_b32 m0, s26
	s_nop 0
	global_load_lds_dwordx4 v221, s[56:57]

.Lu1_5:
	s_waitcnt lgkmcnt(14)
	v_mfma_f32_32x32x16_f16 v[2:17], v[158:161], v[126:129], v[2:17]
	v_exp_f32_e32 v66, v66
	v_exp_f32_e32 v67, v67
	v_exp_f32_e32 v68, v68
	v_exp_f32_e32 v69, v69
	s_waitcnt lgkmcnt(12)
	v_mfma_f32_32x32x16_f16 v[18:33], v[158:161], v[122:125], v[18:33]
	v_exp_f32_e32 v70, v70
	v_exp_f32_e32 v71, v71
	v_exp_f32_e32 v72, v72
	v_exp_f32_e32 v73, v73
	ds_read_b128 v[82:85], v211 offset:16384
	ds_read_b128 v[170:173], v211 offset:20480
	s_waitcnt lgkmcnt(12)
	v_mfma_f32_32x32x16_f16 v[2:17], v[150:153], v[118:121], v[2:17]
	v_exp_f32_e32 v74, v74
	v_exp_f32_e32 v75, v75
	v_exp_f32_e32 v76, v76
	v_exp_f32_e32 v77, v77
	ds_read_b128 v[166:169], v210 offset:16384
	ds_read_b128 v[162:165], v210 offset:20480
	s_waitcnt lgkmcnt(12)
	v_mfma_f32_32x32x16_f16 v[18:33], v[150:153], v[114:117], v[18:33]
	v_exp_f32_e32 v78, v78
	v_exp_f32_e32 v79, v79
	v_exp_f32_e32 v80, v80
	v_exp_f32_e32 v81, v81
	ds_read_b128 v[126:129], v209 offset:16384
	ds_read_b128 v[122:125], v209 offset:20480
	s_waitcnt lgkmcnt(12)
	v_mfma_f32_32x32x16_f16 v[2:17], v[142:145], v[106:109], v[2:17]
	v_exp_f32_e32 v50, v50
	v_exp_f32_e32 v51, v51
	v_exp_f32_e32 v52, v52
	v_exp_f32_e32 v53, v53
	ds_read_b128 v[118:121], v208 offset:16384
	ds_read_b128 v[114:117], v208 offset:20480
	s_waitcnt lgkmcnt(12)
	v_mfma_f32_32x32x16_f16 v[18:33], v[142:145], v[102:105], v[18:33]
	v_exp_f32_e32 v54, v54
	v_exp_f32_e32 v55, v55
	v_exp_f32_e32 v56, v56
	v_exp_f32_e32 v57, v57
	s_waitcnt lgkmcnt(10)
	v_mfma_f32_32x32x16_f16 v[2:17], v[130:133], v[98:101], v[2:17]
	v_exp_f32_e32 v58, v58
	v_exp_f32_e32 v59, v59
	v_exp_f32_e32 v60, v60
	v_exp_f32_e32 v61, v61
	s_waitcnt lgkmcnt(8)
	v_mfma_f32_32x32x16_f16 v[18:33], v[130:133], v[86:89], v[18:33]
	v_exp_f32_e32 v62, v62
	v_exp_f32_e32 v63, v63
	v_exp_f32_e32 v64, v64
	v_exp_f32_e32 v65, v65
	s_cmp_lg_u32 s47, 0
	s_cbranch_scc1 .Ldw4_o
	s_waitcnt vmcnt(4) lgkmcnt(0)
	s_branch .Ldw4_j

.Lu2_1:
	ds_read_b64_tr_b16 v[178:179], v206 offset:32768
	ds_read_b64_tr_b16 v[180:181], v206 offset:33792
	s_waitcnt lgkmcnt(9)
	v_mfma_f32_32x32x16_f16 v[98:113], v[82:85], v[154:157], v[34:49]
	v_add_f32_e32 v86, v66, v67
	v_add_f32_e32 v86, v68, v86
	v_add_f32_e32 v86, v69, v86
	v_add_f32_e32 v86, v70, v86
	v_add_f32_e32 v86, v71, v86
	v_cvt_pk_f16_f32 v158, v66, v67
	v_cvt_pk_f16_f32 v159, v68, v69
	ds_read_b64_tr_b16 v[174:175], v207 offset:32768
	ds_read_b64_tr_b16 v[176:177], v207 offset:33792
	v_add_f32_e32 v66, v72, v86
	s_waitcnt lgkmcnt(10)
	v_mfma_f32_32x32x16_f16 v[82:97], v[170:173], v[154:157], v[34:49]
	v_add_f32_e32 v66, v73, v66
	v_add_f32_e32 v66, v74, v66
	v_add_f32_e32 v66, v75, v66
	v_cvt_pk_f16_f32 v160, v70, v71
	v_cvt_pk_f16_f32 v161, v72, v73
	ds_read_b64_tr_b16 v[170:171], v206 offset:34816
	ds_read_b64_tr_b16 v[172:173], v206 offset:35840
	s_waitcnt lgkmcnt(11)
	v_mfma_f32_32x32x16_f16 v[98:113], v[166:169], v[146:149], v[98:113]
	v_add_f32_e32 v66, v76, v66
	v_add_f32_e32 v66, v77, v66
	v_add_f32_e32 v66, v78, v66
	v_add_f32_e32 v66, v79, v66
	v_cvt_pk_f16_f32 v150, v74, v75
	v_cvt_pk_f16_f32 v151, v76, v77
	ds_read_b64_tr_b16 v[74:75], v207 offset:34816
	ds_read_b64_tr_b16 v[76:77], v207 offset:35840
	s_waitcnt lgkmcnt(12)
	v_mfma_f32_32x32x16_f16 v[82:97], v[162:165], v[146:149], v[82:97]
	v_add_f32_e32 v66, v80, v66
	v_add_f32_e32 v66, v81, v66
	v_add_f32_e32 v66, v50, v66
	v_add_f32_e32 v66, v51, v66
	v_cvt_pk_f16_f32 v152, v78, v79
	v_cvt_pk_f16_f32 v153, v80, v81
	ds_read_b64_tr_b16 v[70:71], v206 offset:36864
	ds_read_b64_tr_b16 v[72:73], v206 offset:37888
	s_waitcnt lgkmcnt(13)
	v_mfma_f32_32x32x16_f16 v[98:113], v[126:129], v[138:141], v[98:113]
	v_add_f32_e32 v66, v52, v66
	v_add_f32_e32 v66, v53, v66
	v_add_f32_e32 v66, v54, v66
	v_add_f32_e32 v78, v55, v66
	v_cvt_pk_f16_f32 v142, v50, v51
	v_cvt_pk_f16_f32 v143, v52, v53
	ds_read_b64_tr_b16 v[66:67], v207 offset:36864
	ds_read_b64_tr_b16 v[68:69], v207 offset:37888
	s_waitcnt lgkmcnt(14)
	v_mfma_f32_32x32x16_f16 v[82:97], v[122:125], v[138:141], v[82:97]
	v_add_f32_e32 v50, v56, v78
	v_add_f32_e32 v50, v57, v50
	v_add_f32_e32 v50, v58, v50
	v_add_f32_e32 v50, v59, v50
	v_cvt_pk_f16_f32 v144, v54, v55
	v_cvt_pk_f16_f32 v145, v56, v57
	ds_read_b64_tr_b16 v[54:55], v206 offset:38912
	ds_read_b64_tr_b16 v[56:57], v206 offset:39936
	s_waitcnt lgkmcnt(14)
	v_mfma_f32_32x32x16_f16 v[98:113], v[118:121], v[134:137], v[98:113]
	v_add_f32_e32 v50, v60, v50
	v_add_f32_e32 v50, v61, v50
	v_add_f32_e32 v50, v62, v50
	v_add_f32_e32 v78, v63, v50
	v_cvt_pk_f16_f32 v130, v58, v59
	v_cvt_pk_f16_f32 v131, v60, v61
	ds_read_b64_tr_b16 v[50:51], v207 offset:38912
	ds_read_b64_tr_b16 v[52:53], v207 offset:39936
	v_mfma_f32_32x32x16_f16 v[82:97], v[114:117], v[134:137], v[82:97]
	v_add_f32_e32 v58, v64, v78
	v_add_f32_e32 v60, v65, v58
	v_cvt_pk_f16_f32 v132, v62, v63
	v_cvt_pk_f16_f32 v133, v64, v65
	s_cmp_lg_u32 s47, 0
	s_cbranch_scc1 .Ldh7_skip
	s_add_i32 s26, s42, s36
	s_mov_b32 m0, s26
	s_nop 0
	global_load_lds_dwordx4 v221, s[50:51]
	s_add_u32 s56, s50, 0x1000
	s_addc_u32 s57, s51, 0
	s_add_i32 s26, s26, 0x1000
	s_mov_b32 m0, s26
	s_nop 0
	global_load_lds_dwordx4 v221, s[56:57]
	s_add_i32 s26, s39, s35
	s_mov_b32 m0, s26
	s_nop 0
	global_load_lds_dwordx4 v222, s[52:53]
	s_add_u32 s56, s52, 0x1000
	s_addc_u32 s57, s53, 0
	s_add_i32 s26, s26, 0x1000
	s_mov_b32 m0, s26
	s_nop 0
	global_load_lds_dwordx4 v222, s[56:57]

.Lu2_2:
	s_waitcnt lgkmcnt(14)
	v_mfma_f32_32x32x16_f16 v[2:17], v[158:161], v[178:181], v[2:17]
	v_exp_f32_e32 v98, v98
	v_exp_f32_e32 v99, v99
	v_exp_f32_e32 v100, v100
	v_exp_f32_e32 v101, v101
	s_waitcnt lgkmcnt(12)
	v_mfma_f32_32x32x16_f16 v[18:33], v[158:161], v[174:177], v[18:33]
	v_exp_f32_e32 v102, v102
	v_exp_f32_e32 v103, v103
	v_exp_f32_e32 v104, v104
	v_exp_f32_e32 v105, v105
	ds_read_b128 v[58:61], v211
	ds_read_b128 v[114:117], v211 offset:4096
	s_waitcnt lgkmcnt(12)
	v_mfma_f32_32x32x16_f16 v[2:17], v[150:153], v[170:173], v[2:17]
	v_exp_f32_e32 v106, v106
	v_exp_f32_e32 v107, v107
	v_exp_f32_e32 v108, v108
	v_exp_f32_e32 v109, v109
	ds_read_b128 v[182:185], v210
	ds_read_b128 v[174:177], v210 offset:4096
	s_waitcnt lgkmcnt(12)
	v_mfma_f32_32x32x16_f16 v[18:33], v[150:153], v[74:77], v[18:33]
	v_exp_f32_e32 v110, v110
	v_exp_f32_e32 v111, v111
	v_exp_f32_e32 v112, v112
	v_exp_f32_e32 v113, v113
	ds_read_b128 v[178:181], v209
	ds_read_b128 v[166:169], v209 offset:4096
	s_waitcnt lgkmcnt(12)
	v_mfma_f32_32x32x16_f16 v[2:17], v[142:145], v[70:73], v[2:17]
	v_exp_f32_e32 v82, v82
	v_exp_f32_e32 v83, v83
	v_exp_f32_e32 v84, v84
	v_exp_f32_e32 v85, v85
	ds_read_b128 v[170:173], v208
	ds_read_b128 v[162:165], v208 offset:4096
	s_waitcnt lgkmcnt(12)
	v_mfma_f32_32x32x16_f16 v[18:33], v[142:145], v[66:69], v[18:33]
	v_exp_f32_e32 v86, v86
	v_exp_f32_e32 v87, v87
	v_exp_f32_e32 v88, v88
	v_exp_f32_e32 v89, v89
	s_waitcnt lgkmcnt(10)
	v_mfma_f32_32x32x16_f16 v[2:17], v[130:133], v[54:57], v[2:17]
	v_exp_f32_e32 v90, v90
	v_exp_f32_e32 v91, v91
	v_exp_f32_e32 v92, v92
	v_exp_f32_e32 v93, v93
	s_waitcnt lgkmcnt(8)
	v_mfma_f32_32x32x16_f16 v[18:33], v[130:133], v[50:53], v[18:33]
	v_exp_f32_e32 v94, v94
	v_exp_f32_e32 v95, v95
	v_exp_f32_e32 v96, v96
	v_exp_f32_e32 v97, v97
	s_cmp_lg_u32 s47, 0
	s_cbranch_scc1 .Ldw5_o
	s_waitcnt vmcnt(4) lgkmcnt(0)
	s_branch .Ldw5_j

.Lu2_4:
	s_add_i32 s26, s39, 0x2000
	s_cmpk_lg_i32 s39, 0x4000
	s_cselect_b32 s43, s26, 0
	ds_read_b64_tr_b16 v[126:127], v206 offset:40960
	ds_read_b64_tr_b16 v[128:129], v206 offset:41984
	s_waitcnt lgkmcnt(9)
	v_mfma_f32_32x32x16_f16 v[66:81], v[58:61], v[154:157], v[34:49]
	v_add_f32_e32 v50, v98, v99
	v_add_f32_e32 v50, v100, v50
	v_add_f32_e32 v50, v101, v50
	v_add_f32_e32 v50, v102, v50
	v_add_f32_e32 v50, v103, v50
	v_cvt_pk_f16_f32 v158, v98, v99
	v_cvt_pk_f16_f32 v159, v100, v101
	ds_read_b64_tr_b16 v[122:123], v207 offset:40960
	ds_read_b64_tr_b16 v[124:125], v207 offset:41984
	v_add_f32_e32 v50, v104, v50
	v_add_f32_e32 v50, v105, v50
	v_add_f32_e32 v50, v106, v50
	v_add_f32_e32 v98, v107, v50
	s_waitcnt lgkmcnt(10)
	v_mfma_f32_32x32x16_f16 v[50:65], v[114:117], v[154:157], v[34:49]
	v_cvt_pk_f16_f32 v160, v102, v103
	v_cvt_pk_f16_f32 v161, v104, v105
	ds_read_b64_tr_b16 v[118:119], v206 offset:43008
	ds_read_b64_tr_b16 v[120:121], v206 offset:44032
	s_waitcnt lgkmcnt(11)
	v_mfma_f32_32x32x16_f16 v[66:81], v[182:185], v[146:149], v[66:81]
	v_add_f32_e32 v98, v108, v98
	v_add_f32_e32 v98, v109, v98
	v_add_f32_e32 v98, v110, v98
	v_add_f32_e32 v98, v111, v98
	v_cvt_pk_f16_f32 v150, v106, v107
	v_cvt_pk_f16_f32 v151, v108, v109
	ds_read_b64_tr_b16 v[114:115], v207 offset:43008
	ds_read_b64_tr_b16 v[116:117], v207 offset:44032
	s_waitcnt lgkmcnt(12)
	v_mfma_f32_32x32x16_f16 v[50:65], v[174:177], v[146:149], v[50:65]
	v_add_f32_e32 v98, v112, v98
	v_add_f32_e32 v98, v113, v98
	v_add_f32_e32 v98, v82, v98
	v_add_f32_e32 v98, v83, v98
	v_cvt_pk_f16_f32 v152, v110, v111
	v_cvt_pk_f16_f32 v153, v112, v113
	ds_read_b64_tr_b16 v[106:107], v206 offset:45056
	ds_read_b64_tr_b16 v[108:109], v206 offset:46080
	s_waitcnt lgkmcnt(13)
	v_mfma_f32_32x32x16_f16 v[66:81], v[178:181], v[138:141], v[66:81]
	v_add_f32_e32 v98, v84, v98
	v_add_f32_e32 v98, v85, v98
	v_add_f32_e32 v98, v86, v98
	v_add_f32_e32 v98, v87, v98
	v_cvt_pk_f16_f32 v142, v82, v83
	v_cvt_pk_f16_f32 v143, v84, v85
	ds_read_b64_tr_b16 v[102:103], v207 offset:45056
	ds_read_b64_tr_b16 v[104:105], v207 offset:46080
	s_waitcnt lgkmcnt(14)
	v_mfma_f32_32x32x16_f16 v[50:65], v[166:169], v[138:141], v[50:65]
	v_add_f32_e32 v82, v88, v98
	v_add_f32_e32 v82, v89, v82
	v_add_f32_e32 v82, v90, v82
	v_add_f32_e32 v82, v91, v82
	v_cvt_pk_f16_f32 v144, v86, v87
	v_cvt_pk_f16_f32 v145, v88, v89
	ds_read_b64_tr_b16 v[98:99], v206 offset:47104
	ds_read_b64_tr_b16 v[100:101], v206 offset:48128
	s_waitcnt lgkmcnt(14)
	v_mfma_f32_32x32x16_f16 v[66:81], v[170:173], v[134:137], v[66:81]
	v_add_f32_e32 v82, v92, v82
	v_add_f32_e32 v82, v93, v82
	v_add_f32_e32 v82, v94, v82
	v_add_f32_e32 v82, v95, v82
	v_cvt_pk_f16_f32 v130, v90, v91
	v_cvt_pk_f16_f32 v131, v92, v93
	ds_read_b64_tr_b16 v[86:87], v207 offset:47104
	ds_read_b64_tr_b16 v[88:89], v207 offset:48128
	v_mfma_f32_32x32x16_f16 v[50:65], v[162:165], v[134:137], v[50:65]
	v_add_f32_e32 v82, v96, v82
	v_add_f32_e32 v84, v97, v82
	v_cvt_pk_f16_f32 v132, v94, v95
	v_cvt_pk_f16_f32 v133, v96, v97
	s_cmp_lg_u32 s47, 0
	s_cbranch_scc1 .Ldh8_skip
	s_add_u32 s54, s50, 0x2000
	s_addc_u32 s55, s51, 0
	s_add_i32 s26, s39, s36
	s_mov_b32 m0, s26
	s_nop 0
	global_load_lds_dwordx4 v221, s[54:55]
	s_add_u32 s56, s54, 0x1000
	s_addc_u32 s57, s55, 0
	s_add_i32 s26, s26, 0x1000
	s_mov_b32 m0, s26
	s_nop 0
	global_load_lds_dwordx4 v221, s[56:57]

.Lu2_5:
	s_waitcnt lgkmcnt(14)
	v_mfma_f32_32x32x16_f16 v[2:17], v[158:161], v[126:129], v[2:17]
	v_exp_f32_e32 v66, v66
	v_exp_f32_e32 v67, v67
	v_exp_f32_e32 v68, v68
	v_exp_f32_e32 v69, v69
	s_waitcnt lgkmcnt(12)
	v_mfma_f32_32x32x16_f16 v[18:33], v[158:161], v[122:125], v[18:33]
	v_exp_f32_e32 v70, v70
	v_exp_f32_e32 v71, v71
	v_exp_f32_e32 v72, v72
	v_exp_f32_e32 v73, v73
	ds_read_b128 v[82:85], v211 offset:8192
	ds_read_b128 v[170:173], v211 offset:12288
	s_waitcnt lgkmcnt(12)
	v_mfma_f32_32x32x16_f16 v[2:17], v[150:153], v[118:121], v[2:17]
	v_exp_f32_e32 v74, v74
	v_exp_f32_e32 v75, v75
	v_exp_f32_e32 v76, v76
	v_exp_f32_e32 v77, v77
	ds_read_b128 v[166:169], v210 offset:8192
	ds_read_b128 v[162:165], v210 offset:12288
	s_waitcnt lgkmcnt(12)
	v_mfma_f32_32x32x16_f16 v[18:33], v[150:153], v[114:117], v[18:33]
	v_exp_f32_e32 v78, v78
	v_exp_f32_e32 v79, v79
	v_exp_f32_e32 v80, v80
	v_exp_f32_e32 v81, v81
	ds_read_b128 v[126:129], v209 offset:8192
	ds_read_b128 v[122:125], v209 offset:12288
	s_waitcnt lgkmcnt(12)
	v_mfma_f32_32x32x16_f16 v[2:17], v[142:145], v[106:109], v[2:17]
	v_exp_f32_e32 v50, v50
	v_exp_f32_e32 v51, v51
	v_exp_f32_e32 v52, v52
	v_exp_f32_e32 v53, v53
	ds_read_b128 v[118:121], v208 offset:8192
	ds_read_b128 v[114:117], v208 offset:12288
	s_waitcnt lgkmcnt(12)
	v_mfma_f32_32x32x16_f16 v[18:33], v[142:145], v[102:105], v[18:33]
	v_exp_f32_e32 v54, v54
	v_exp_f32_e32 v55, v55
	v_exp_f32_e32 v56, v56
	v_exp_f32_e32 v57, v57
	s_waitcnt lgkmcnt(10)
	v_mfma_f32_32x32x16_f16 v[2:17], v[130:133], v[98:101], v[2:17]
	v_exp_f32_e32 v58, v58
	v_exp_f32_e32 v59, v59
	v_exp_f32_e32 v60, v60
	v_exp_f32_e32 v61, v61
	s_waitcnt lgkmcnt(8)
	v_mfma_f32_32x32x16_f16 v[18:33], v[130:133], v[86:89], v[18:33]
	v_exp_f32_e32 v62, v62
	v_exp_f32_e32 v63, v63
	v_exp_f32_e32 v64, v64
	v_exp_f32_e32 v65, v65
	s_cmp_lg_u32 s47, 0
	s_cbranch_scc1 .Ldw6_o
	s_waitcnt vmcnt(4) lgkmcnt(0)
	s_branch .Ldw6_j

.Ldh1_skip:
	s_nop 5
	s_branch .Ldh1_join

.Lattn_unit2:
	s_load_dwordx4 s[4:7], s[0:1], 0x0
	s_lshr_b32 s0, s2, 2
	s_and_b32 s3, s2, 7
	s_and_b32 s0, s0, 8
	s_or_b32 s30, s0, s3
	s_lshr_b32 s18, s2, 6
	s_mov_b32 s19, 0
	s_lshl_b32 s0, s2, 5
	v_readfirstlane_b32 s16, v0
	s_and_b32 s12, s0, 0x300
	s_xor_b32 s12, s12, s91
	s_lshl_b64 s[8:9], s[18:19], 15
	s_lshl_b32 s0, s30, 11
	s_lshr_b32 s33, s16, 6
	s_bfe_u32 s47, s16, 0x10008
	s_or_b32 s8, s8, s0
	s_or_b32 s0, s8, s12
	s_lshl_b32 s31, s33, 5
	s_add_u32 s0, s0, s31
	s_addc_u32 s1, s9, 0
	s_lshl_b64 s[0:1], s[0:1], 7
	s_waitcnt lgkmcnt(0)
	s_add_u32 s0, s4, s0
	s_addc_u32 s1, s5, s1
	s_lshl_b64 s[10:11], s[8:9], 7
	v_bfe_u32 v190, v0, 3, 3
	s_add_u32 s10, s4, s10
	v_lshl_or_b32 v182, s33, 3, v190
	s_addc_u32 s11, s5, s11
	v_lshrrev_b32_e32 v89, 1, v182
	s_add_u32 s14, s10, 0x1000000
	v_xor_b32_e32 v4, v89, v0
	s_addc_u32 s15, s11, 0
	v_mov_b32_e32 v183, 0
	v_lshlrev_b32_e32 v4, 4, v4
	s_add_u32 s10, s10, 0x2000000
	v_lshlrev_b64 v[86:87], 7, v[182:183]
	v_and_b32_e32 v1, 7, v0
	v_and_b32_e32 v182, 0x70, v4
	v_lshrrev_b32_e32 v4, 2, v0
	s_addc_u32 s11, s11, 0
	v_lshl_add_u64 v[2:3], s[14:15], 0, v[86:87]
	v_bitop3_b32 v4, v4, v1, 4 bitop3:0x6c
	v_lshl_add_u64 v[186:187], v[2:3], 0, v[182:183]
	v_lshl_add_u64 v[2:3], s[10:11], 0, v[86:87]
	v_lshlrev_b32_e32 v182, 4, v4
	s_lshl_b32 s36, s33, 10
	s_mov_b64 s[20:21], 0x2000
	v_and_b32_e32 v191, 31, v0
	v_lshl_add_u64 v[194:195], v[2:3], 0, v[182:183]
	s_add_i32 s35, s36, 0x6000
	v_lshl_add_u64 v[2:3], v[186:187], 0, s[20:21]
	v_bfe_u32 v88, v0, 5, 1
	s_add_i32 s37, s36, 0x2000
	v_lshlrev_b32_e32 v2, 6, v191
	v_lshl_or_b32 v192, v88, 3, v2
	v_lshlrev_b32_e32 v14, 1, v192
	v_lshrrev_b32_e32 v18, 1, v0
	s_mov_b64 s[22:23], 0x4000
	v_mov_b32_e32 v2, v183
	v_mov_b32_e32 v3, v183
	v_mov_b32_e32 v4, v183
	v_mov_b32_e32 v5, v183
	v_mov_b32_e32 v6, v183
	v_mov_b32_e32 v7, v183
	v_mov_b32_e32 v8, v183
	v_mov_b32_e32 v9, v183
	v_mov_b32_e32 v10, v183
	v_mov_b32_e32 v11, v183
	v_mov_b32_e32 v12, v183
	v_mov_b32_e32 v13, v183
	v_mov_b32_e32 v14, v183
	v_mov_b32_e32 v15, v183
	v_mov_b32_e32 v16, v183
	v_mov_b32_e32 v17, v183
	v_lshlrev_b32_e32 v38, 7, v191
	v_bitop3_b32 v18, v88, v18, 7 bitop3:0x78
	v_lshl_or_b32 v211, v18, 4, v38
	v_lshl_add_u64 v[18:19], v[186:187], 0, s[22:23]
	s_add_i32 s0, s36, 0x4000
	s_waitcnt vmcnt(4) lgkmcnt(0)
	s_barrier
	ds_read_b128 v[34:37], v211
	v_bfe_u32 v39, v0, 1, 3
	v_bitop3_b32 v40, v88, v39, 2 bitop3:0x36
	v_lshl_or_b32 v210, v40, 4, v38
	v_bitop3_b32 v40, v88, v39, 4 bitop3:0x36
	v_lshl_or_b32 v209, v40, 4, v38
	v_bitop3_b32 v39, v88, v39, 6 bitop3:0x36
	v_lshl_or_b32 v208, v39, 4, v38
	v_lshlrev_b32_e32 v201, 9, v88
	s_and_b32 s0, s16, 0x3fffffc0
	s_mov_b64 s[24:25], 0x6000
	s_lshl_b32 s38, s0, 2
	s_add_i32 s34, s36, 0x8000
	s_lshl_b32 s2, s2, 16
	s_lshl_b32 s3, s3, 18
	s_waitcnt vmcnt(4) lgkmcnt(0)
	v_mfma_f32_32x32x16_f16 v[18:33], v[34:37], v[154:157], v[2:17]
	ds_read_b128 v[34:37], v211 offset:4096
	s_and_b32 s2, s2, 0x200000
	s_lshl_b64 s[16:17], s[18:19], 22
	s_or_b32 s2, s2, s3
	s_or_b32 s16, s16, s2
	s_mov_b64 s[2:3], 0x1002000
	v_and_b32_e32 v90, 63, v0
	s_waitcnt lgkmcnt(0)
	v_mfma_f32_32x32x16_f16 v[2:17], v[34:37], v[154:157], v[2:17]
	ds_read_b128 v[34:37], v210
	s_mov_b32 s13, s19
	s_movk_i32 s42, 0x2000
	s_movk_i32 s39, 0x4000
	v_lshl_or_b32 v204, v191, 2, s38
	v_lshlrev_b32_e32 v212, 4, v88
	s_mov_b32 s40, -1
	s_waitcnt vmcnt(4) lgkmcnt(0)
	v_mfma_f32_32x32x16_f16 v[18:33], v[34:37], v[146:149], v[18:33]
	ds_read_b128 v[34:37], v210 offset:4096
	s_mov_b32 s41, 0x41000000
	s_mov_b32 s26, s19
	s_waitcnt lgkmcnt(0)
	v_mfma_f32_32x32x16_f16 v[2:17], v[34:37], v[146:149], v[2:17]
	ds_read_b128 v[34:37], v209
	s_waitcnt vmcnt(4) lgkmcnt(0)
	v_mfma_f32_32x32x16_f16 v[18:33], v[34:37], v[138:141], v[18:33]
	ds_read_b128 v[34:37], v209 offset:4096
	ds_read_b128 v[38:41], v208 offset:4096
	ds_read_b128 v[42:45], v208
	s_waitcnt lgkmcnt(2)
	v_mfma_f32_32x32x16_f16 v[2:17], v[34:37], v[138:141], v[2:17]
	v_lshlrev_b32_e32 v34, 5, v0
	v_lshlrev_b32_e32 v35, 1, v0
	v_lshlrev_b32_e32 v36, 3, v0
	v_and_b32_e32 v34, 0x180, v34
	v_and_b32_e32 v193, 24, v36
	v_and_or_b32 v34, v35, 32, v34
	v_or3_b32 v203, v34, v193, v201
	s_waitcnt vmcnt(4) lgkmcnt(0)
	v_mfma_f32_32x32x16_f16 v[18:33], v[42:45], v[134:137], v[18:33]
	v_and_b32_e32 v200, 64, v36
	v_bitop3_b32 v202, v36, 64, v36 bitop3:0xc
	v_or_b32_e32 v206, v203, v200
	v_or_b32_e32 v207, v203, v202
	v_mfma_f32_32x32x16_f16 v[2:17], v[38:41], v[134:137], v[2:17]
	s_nop 15
	s_nop 7
	s_nop 0
	v_max3_f32 v34, v18, v19, v2
	v_max3_f32 v35, v20, v21, v3
	s_nop 0
	v_max3_f32 v34, v34, v4, v5
	v_max3_f32 v35, v35, v24, v25
	s_nop 0
	v_max3_f32 v34, v34, v22, v23
	v_max3_f32 v35, v35, v8, v9
	s_nop 0
	v_max3_f32 v34, v34, v6, v7
	v_max3_f32 v35, v35, v28, v29
	s_nop 0
	v_max3_f32 v34, v34, v26, v27
	v_max3_f32 v35, v35, v12, v13
	s_nop 0
	v_max3_f32 v34, v34, v10, v11
	v_max3_f32 v35, v35, v32, v33
	s_nop 0
	v_max3_f32 v34, v34, v30, v31
	v_max3_f32 v35, v35, v16, v17
	s_nop 0
	v_max3_f32 v34, v34, v14, v15
	s_nop 0
	v_max_f32_e32 v34, v34, v35
	s_nop 0
	v_mov_b32_e32 v35, v34
	s_nop 1
	v_permlane32_swap_b32_e32 v34, v35
	v_max_f32_e32 v34, v34, v35
	s_nop 0
	v_add_f32_e32 v205, v183, v34
	v_sub_f32_e32 v18, v18, v34
	v_sub_f32_e32 v2, v2, v34
	v_sub_f32_e32 v19, v19, v34
	v_sub_f32_e32 v3, v3, v34
	v_sub_f32_e32 v20, v20, v34
	v_sub_f32_e32 v4, v4, v34
	v_sub_f32_e32 v21, v21, v34
	v_sub_f32_e32 v5, v5, v34
	v_sub_f32_e32 v22, v22, v34
	v_sub_f32_e32 v6, v6, v34
	v_sub_f32_e32 v23, v23, v34
	v_sub_f32_e32 v7, v7, v34
	v_sub_f32_e32 v24, v24, v34
	v_sub_f32_e32 v8, v8, v34
	v_sub_f32_e32 v25, v25, v34
	v_sub_f32_e32 v9, v9, v34
	v_sub_f32_e32 v26, v26, v34
	v_sub_f32_e32 v10, v10, v34
	v_sub_f32_e32 v27, v27, v34
	v_sub_f32_e32 v11, v11, v34
	v_sub_f32_e32 v28, v28, v34
	v_sub_f32_e32 v12, v12, v34
	v_sub_f32_e32 v29, v29, v34
	v_sub_f32_e32 v13, v13, v34
	v_sub_f32_e32 v30, v30, v34
	v_sub_f32_e32 v14, v14, v34
	v_sub_f32_e32 v31, v31, v34
	v_sub_f32_e32 v15, v15, v34
	v_sub_f32_e32 v32, v32, v34
	v_sub_f32_e32 v16, v16, v34
	v_sub_f32_e32 v33, v33, v34
	v_sub_f32_e32 v17, v17, v34
	s_nop 0
	v_xor_b32_e32 v34, 0x80000000, v205
	v_mov_b32_e32 v35, v34
	v_mov_b32_e32 v36, v34
	v_mov_b32_e32 v37, v34
	v_mov_b32_e32 v38, v34
	v_mov_b32_e32 v39, v34
	v_mov_b32_e32 v40, v34
	v_mov_b32_e32 v41, v34
	v_mov_b32_e32 v42, v34
	v_mov_b32_e32 v43, v34
	v_mov_b32_e32 v44, v34
	v_mov_b32_e32 v45, v34
	v_mov_b32_e32 v46, v34
	v_mov_b32_e32 v47, v34
	v_mov_b32_e32 v48, v34
	v_mov_b32_e32 v49, v34
	s_waitcnt vmcnt(0) lgkmcnt(0)
	s_barrier
	v_exp_f32_e32 v50, v2
	v_exp_f32_e32 v51, v3
	v_lshl_add_u64 v[2:3], v[186:187], 0, s[24:25]
	s_mov_b32 s0, m0
	s_mov_b32 m0, s36
	s_nop 0
	global_load_lds_dwordx4 v[2:3], off
	s_mov_b32 m0, s0
	v_lshl_add_u64 v[2:3], v[194:195], 0, s[20:21]
	s_mov_b32 s0, m0
	s_mov_b32 m0, s34
	s_nop 0
	global_load_lds_dwordx4 v[2:3], off
	s_mov_b32 m0, s0
	ds_read_b128 v[82:85], v211 offset:8192
	ds_read_b128 v[170:173], v211 offset:12288
	ds_read_b128 v[166:169], v210 offset:8192
	ds_read_b128 v[162:165], v210 offset:12288
	ds_read_b128 v[126:129], v209 offset:8192
	ds_read_b128 v[122:125], v209 offset:12288
	ds_read_b128 v[118:121], v208 offset:8192
	ds_read_b128 v[114:117], v208 offset:12288
	v_exp_f32_e32 v52, v4
	v_lshl_add_u64 v[2:3], s[16:17], 0, v[86:87]
	v_bitop3_b32 v4, v89, 7, v0 bitop3:0x48
	v_exp_f32_e32 v66, v18
	v_exp_f32_e32 v67, v19
	v_exp_f32_e32 v68, v20
	v_exp_f32_e32 v69, v21
	v_exp_f32_e32 v70, v22
	v_exp_f32_e32 v71, v23
	v_exp_f32_e32 v72, v24
	v_exp_f32_e32 v73, v25
	v_exp_f32_e32 v74, v26
	v_exp_f32_e32 v75, v27
	v_exp_f32_e32 v76, v28
	v_exp_f32_e32 v77, v29
	v_exp_f32_e32 v78, v30
	v_exp_f32_e32 v79, v31
	v_exp_f32_e32 v80, v32
	v_exp_f32_e32 v81, v33
	v_exp_f32_e32 v53, v5
	v_exp_f32_e32 v54, v6
	v_exp_f32_e32 v55, v7
	v_exp_f32_e32 v56, v8
	v_exp_f32_e32 v57, v9
	v_exp_f32_e32 v58, v10
	v_exp_f32_e32 v59, v11
	v_exp_f32_e32 v60, v12
	v_exp_f32_e32 v61, v13
	v_exp_f32_e32 v62, v14
	v_exp_f32_e32 v63, v15
	v_exp_f32_e32 v64, v16
	v_exp_f32_e32 v65, v17
	v_lshl_or_b32 v4, v4, 4, v2
	v_mov_b32_e32 v5, v3
	s_waitcnt vmcnt(2) lgkmcnt(0)
	s_barrier
	v_lshl_add_u64 v[4:5], s[4:5], 0, v[4:5]
	v_or_b32_e32 v2, v2, v182
	v_lshl_add_u64 v[188:189], v[4:5], 0, s[2:3]
	v_lshl_add_u64 v[2:3], s[4:5], 0, v[2:3]
	s_mov_b64 s[2:3], 0x2002000
	v_cmp_gt_u32_e64 s[0:1], 32, v90
	v_lshl_add_u64 v[196:197], v[2:3], 0, s[2:3]
	s_mov_b64 s[2:3], 0x8000
	v_mov_b32_e32 v2, v183
	v_mov_b32_e32 v3, v183
	v_mov_b32_e32 v4, v183
	v_mov_b32_e32 v5, v183
	v_mov_b32_e32 v6, v183
	v_mov_b32_e32 v7, v183
	v_mov_b32_e32 v8, v183
	v_mov_b32_e32 v9, v183
	v_mov_b32_e32 v10, v183
	v_mov_b32_e32 v11, v183
	v_mov_b32_e32 v12, v183
	v_mov_b32_e32 v13, v183
	v_mov_b32_e32 v14, v183
	v_mov_b32_e32 v15, v183
	v_mov_b32_e32 v16, v183
	v_mov_b32_e32 v17, v183
	v_mov_b32_e32 v18, v183
	v_mov_b32_e32 v19, v183
	v_mov_b32_e32 v20, v183
	v_mov_b32_e32 v21, v183
	v_mov_b32_e32 v22, v183
	v_mov_b32_e32 v23, v183
	v_mov_b32_e32 v24, v183
	v_mov_b32_e32 v25, v183
	v_mov_b32_e32 v26, v183
	v_mov_b32_e32 v27, v183
	v_mov_b32_e32 v28, v183
	v_mov_b32_e32 v29, v183
	v_mov_b32_e32 v30, v183
	v_mov_b32_e32 v31, v183
	v_mov_b32_e32 v32, v183
	v_mov_b32_e32 v33, v183
	v_subrev_u32_e32 v221, s14, v186
	v_subrev_u32_e32 v222, s10, v194
	s_add_u32 s50, s14, 0x8000
	s_addc_u32 s51, s15, 0
	s_add_u32 s52, s10, 0x4000
	s_addc_u32 s53, s11, 0
	s_branch .Lu0_1
